# speedup vs baseline: 1.0752x; 1.0752x over previous
.LBB1_15:
	v_readfirstlane_b32 s86, v172
	v_readfirstlane_b32 s87, v173
	v_readfirstlane_b32 s88, v174
	v_readfirstlane_b32 s89, v175
	v_lshrrev_b32_e32 v232, 3, v198
	v_and_b32_e32 v233, 7, v198
	v_xor_b32_e32 v233, v233, v232
	s_and_b32 s84, s27, 0x7ff
	s_lshr_b32 s85, s62, 1
	s_lshl_b32 s85, s85, 7
	s_add_i32 s84, s84, s85
	s_and_b32 s85, s62, 1
	s_lshl_b32 s85, s85, 5
	s_add_i32 s84, s84, s85
	v_add_u32_e32 v232, s84, v232
	v_lshlrev_b32_e32 v232, 7, v232
	v_lshl_add_u32 v232, v233, 4, v232
	s_bfe_u32 s91, s27, 0x10006
	s_lshl_b32 s90, s91, 2
	s_add_i32 s90, s90, s62
	s_lshl_b32 s90, s90, 10
	s_add_u32 s92, s86, 0x0
	s_addc_u32 s93, s87, 0
	s_add_i32 m0, s90, 0x0
	s_nop 0
	global_load_lds_dwordx4 v232, s[92:93]
	s_add_u32 s92, s86, 0x400
	s_addc_u32 s93, s87, 0
	s_add_i32 m0, s90, 0x2000
	s_nop 0
	global_load_lds_dwordx4 v232, s[92:93]
	s_add_u32 s92, s86, 0x800
	s_addc_u32 s93, s87, 0
	s_add_i32 m0, s90, 0x4000
	s_nop 0
	global_load_lds_dwordx4 v232, s[92:93]
	s_add_u32 s92, s86, 0xc00
	s_addc_u32 s93, s87, 0
	s_add_i32 m0, s90, 0x6000
	s_nop 0
	global_load_lds_dwordx4 v232, s[92:93]
	s_add_u32 s92, s88, 0x0
	s_addc_u32 s93, s89, 0
	s_add_i32 m0, s90, 0x8000
	s_nop 0
	global_load_lds_dwordx4 v232, s[92:93]
	s_add_u32 s92, s88, 0x400
	s_addc_u32 s93, s89, 0
	s_add_i32 m0, s90, 0xa000
	s_nop 0
	global_load_lds_dwordx4 v232, s[92:93]
	s_add_u32 s92, s88, 0x800
	s_addc_u32 s93, s89, 0
	s_add_i32 m0, s90, 0xc000
	s_nop 0
	global_load_lds_dwordx4 v232, s[92:93]
	s_add_u32 s92, s88, 0xc00
	s_addc_u32 s93, s89, 0
	s_add_i32 m0, s90, 0xe000
	s_nop 0
	global_load_lds_dwordx4 v232, s[92:93]
	v_and_b32_e32 v234, 15, v198
	v_lshrrev_b32_e32 v235, 4, v198
	v_and_b32_e32 v236, 7, v234
	v_lshrrev_b32_e32 v237, 3, v234
	v_lshlrev_b32_e32 v238, 1, v235
	v_xor_b32_e32 v239, v238, v236
	v_or_b32_e32 v238, 1, v238
	v_xor_b32_e32 v238, v238, v236
	v_lshlrev_b32_e32 v237, 13, v237
	v_lshl_add_u32 v237, v236, 7, v237
	s_lshl_b32 s91, s91, 12
	v_add_u32_e32 v237, s91, v237
	v_lshl_add_u32 v244, v239, 4, v237
	v_lshl_add_u32 v245, v238, 4, v237
	s_waitcnt vmcnt(0)
	s_barrier
	s_cmp_gt_i32 s77, 7
	s_cselect_b64 s[52:53], -1, 0
	s_lshl_b32 s4, s77, 2
	s_add_i32 s78, s4, s66
	s_or_b32 s37, s4, s62
	s_lshr_b32 s4, s27, 8
	s_and_b32 s4, s4, 0x7ff8
	v_and_b32_e32 v147, 64, v198
	s_add_i32 s10, s4, s78
	s_lshr_b32 s4, s27, 6
	v_xor_b32_e32 v146, 16, v198
	v_add_u32_e32 v206, 64, v147
	s_and_b32 s4, s4, 0x7fe0
	v_cmp_lt_i32_e32 vcc, v146, v206
	s_add_i32 s54, s4, s37
	s_cmp_lt_i32 s77, 8
	v_cndmask_b32_e32 v146, v198, v146, vcc
	v_lshlrev_b32_e32 v201, 2, v146
	v_mul_f32_e32 v146, v127, v127
	v_mul_f32_e32 v147, v129, v129
	s_cselect_b64 s[6:7], -1, 0
	v_fmac_f32_e32 v146, v126, v126
	v_fmac_f32_e32 v147, v128, v128
	s_and_b64 s[4:5], s[6:7], exec
	v_add_f32_e32 v153, v146, v147
	v_pk_mul_f32 v[146:147], v[124:125], v[124:125]
	v_pk_mul_f32 v[148:149], v[122:123], v[122:123]
	s_cselect_b32 s9, s23, s25
	s_cselect_b32 s8, s22, s24
	v_and_b32_e32 v152, 0x7cf, v199
	v_mov_b32_e32 v150, v146
	v_mov_b32_e32 v151, v148
	v_mov_b32_e32 v148, v147
	global_load_dwordx4 v[138:141], v194, s[8:9] offset:16
	global_load_dwordx4 v[142:145], v194, s[8:9]
	global_load_dwordx4 v[130:133], v194, s[8:9] offset:144
	global_load_dwordx4 v[134:137], v194, s[8:9] offset:128
	v_pk_add_f32 v[146:147], v[150:151], v[148:149]
	v_lshlrev_b32_e32 v170, 7, v152
	v_add_f32_e32 v147, v153, v147
	v_add_f32_e32 v207, v146, v147
	ds_read_b128 v[146:149], v245 offset:32768
	s_nop 0
	ds_read_b128 v[150:153], v244 offset:32768
	s_nop 0
	ds_read_b128 v[154:157], v245 offset:0
	s_nop 0
	ds_read_b128 v[158:161], v244 offset:0
	v_pk_mul_f32 v[184:185], v[112:113], v[112:113]
	v_pk_mul_f32 v[202:203], v[110:111], v[110:111]
	v_mov_b32_e32 v204, v184
	v_mov_b32_e32 v205, v202
	v_mov_b32_e32 v202, v185
	v_pk_add_f32 v[184:185], v[204:205], v[202:203]
	v_pk_mul_f32 v[202:203], v[106:107], v[106:107]
	v_add_f32_e32 v170, v207, v185
	v_add_f32_e32 v170, v184, v170
	v_pk_mul_f32 v[184:185], v[108:109], v[108:109]
	v_mov_b32_e32 v205, v202
	v_mov_b32_e32 v204, v184
	v_mov_b32_e32 v202, v185
	v_pk_add_f32 v[184:185], v[204:205], v[202:203]
	v_cndmask_b32_e64 v200, 1.0, v197, s[6:7]
	v_add_f32_e32 v170, v185, v170
	v_add_f32_e32 v170, v184, v170
	ds_bpermute_b32 v184, v201, v170
	v_xor_b32_e32 v185, 32, v198
	v_cmp_lt_i32_e32 vcc, v185, v206
	s_cselect_b32 s55, s17, s19
	v_or_b32_e32 v229, 16, v199
	v_cndmask_b32_e32 v185, v198, v185, vcc
	v_lshlrev_b32_e32 v202, 2, v185
	s_waitcnt lgkmcnt(0)
	v_add_f32_e32 v170, v170, v184
	ds_bpermute_b32 v184, v202, v170
	s_waitcnt lgkmcnt(0)
	v_add_f32_e32 v170, v170, v184
	v_fmamk_f32 v170, v170, 0x3c800000, v195
	v_mul_f32_e32 v184, 0x4f800000, v170
	v_cmp_gt_f32_e32 vcc, s70, v170
	s_nop 1
	v_cndmask_b32_e32 v170, v170, v184, vcc
	v_sqrt_f32_e32 v184, v170
	s_nop 0
	v_add_u32_e32 v185, -1, v184
	v_fma_f32 v203, -v185, v184, v170
	v_cmp_ge_f32_e64 s[8:9], 0, v203
	v_add_u32_e32 v203, 1, v184
	s_nop 0
	v_cndmask_b32_e64 v185, v184, v185, s[8:9]
	v_fma_f32 v184, -v203, v184, v170
	v_cmp_lt_f32_e64 s[8:9], 0, v184
	s_nop 1
	v_cndmask_b32_e64 v184, v185, v203, s[8:9]
	v_mul_f32_e32 v185, 0x37800000, v184
	v_cndmask_b32_e32 v184, v184, v185, vcc
	v_cmp_class_f32_e32 vcc, v170, v196
	v_lshl_or_b32 v203, s10, 17, v187
	v_lshl_or_b32 v185, s54, 17, v188
	v_cndmask_b32_e32 v170, v184, v170, vcc
	v_div_scale_f32 v184, s[8:9], v170, v170, v200
	v_rcp_f32_e32 v204, v184
	s_cselect_b32 s54, s16, s18
	s_cselect_b32 s10, s72, 0x1000
	v_fma_f32 v205, -v184, v204, 1.0
	v_fmac_f32_e32 v204, v205, v204
	v_div_scale_f32 v205, vcc, v200, v170, v200
	v_mul_f32_e32 v206, v205, v204
	v_fma_f32 v207, -v184, v206, v205
	v_fmac_f32_e32 v206, v207, v204
	v_fma_f32 v184, -v184, v206, v205
	v_div_fmas_f32 v184, v184, v204, v206
	v_div_fixup_f32 v170, v184, v170, v200
	v_pk_mul_f32 v[216:217], v[106:107], v[170:171] op_sel_hi:[1,0]
	v_pk_mul_f32 v[210:211], v[122:123], v[170:171] op_sel_hi:[1,0]
	s_waitcnt vmcnt(0)
	v_pk_mul_f32 v[216:217], v[130:131], v[216:217]
	v_pk_mul_f32 v[210:211], v[138:139], v[210:211]
	v_pk_mul_f32 v[224:225], v[146:147], v[216:217]
	v_pk_mul_f32 v[212:213], v[110:111], v[170:171] op_sel_hi:[1,0]
	v_pk_fma_f32 v[224:225], v[154:155], v[210:211], v[224:225] neg_lo:[0,0,1] neg_hi:[0,0,1]
	v_pk_mul_f32 v[154:155], v[154:155], v[216:217]
	v_pk_mul_f32 v[214:215], v[112:113], v[170:171] op_sel_hi:[1,0]
	v_pk_mul_f32 v[218:219], v[108:109], v[170:171] op_sel_hi:[1,0]
	v_pk_fma_f32 v[154:155], v[146:147], v[210:211], v[154:155]
	v_lshlrev_b32_e32 v146, 6, v199
	v_pk_mul_f32 v[204:205], v[128:129], v[170:171] op_sel_hi:[1,0]
	v_pk_mul_f32 v[206:207], v[126:127], v[170:171] op_sel_hi:[1,0]
	v_pk_mul_f32 v[208:209], v[124:125], v[170:171] op_sel_hi:[1,0]
	v_pk_mul_f32 v[214:215], v[136:137], v[214:215]
	v_pk_mul_f32 v[212:213], v[134:135], v[212:213]
	v_pk_mul_f32 v[218:219], v[132:133], v[218:219]
	v_cndmask_b32_e64 v184, v203, v185, s[6:7]
	v_and_b32_e32 v228, 0x1f000, v146
	v_pk_mul_f32 v[206:207], v[142:143], v[206:207]
	v_pk_mul_f32 v[204:205], v[144:145], v[204:205]
	v_pk_mul_f32 v[208:209], v[140:141], v[208:209]
	v_pk_mul_f32 v[220:221], v[150:151], v[212:213]
	v_pk_mul_f32 v[222:223], v[152:153], v[214:215]
	v_pk_mul_f32 v[226:227], v[148:149], v[218:219]
	v_or3_b32 v146, v228, v189, v184
	v_pk_fma_f32 v[222:223], v[160:161], v[204:205], v[222:223] neg_lo:[0,0,1] neg_hi:[0,0,1]
	v_pk_fma_f32 v[220:221], v[158:159], v[206:207], v[220:221] neg_lo:[0,0,1] neg_hi:[0,0,1]
	v_pk_fma_f32 v[226:227], v[156:157], v[208:209], v[226:227] neg_lo:[0,0,1] neg_hi:[0,0,1]
	v_pk_mul_f32 v[158:159], v[158:159], v[212:213]
	v_pk_mul_f32 v[160:161], v[160:161], v[214:215]
	v_pk_mul_f32 v[156:157], v[156:157], v[218:219]
	v_ashrrev_i32_e32 v147, 31, v146
	v_pk_fma_f32 v[152:153], v[152:153], v[204:205], v[160:161]
	v_pk_fma_f32 v[150:151], v[150:151], v[206:207], v[158:159]
	v_pk_fma_f32 v[156:157], v[148:149], v[208:209], v[156:157]
	v_lshl_add_u64 v[158:159], v[146:147], 1, s[54:55]
	v_cvt_pk_f16_f32 v146, v220, v221
	v_cvt_pk_f16_f32 v147, v222, v223
	v_cvt_pk_f16_f32 v148, v224, v225
	v_cvt_pk_f16_f32 v149, v226, v227
	v_cvt_pk_f16_f32 v150, v150, v151
	v_cvt_pk_f16_f32 v151, v152, v153
	v_cvt_pk_f16_f32 v152, v154, v155
	v_cvt_pk_f16_f32 v153, v156, v157
	global_store_dwordx4 v[158:159], v[146:149], off sc1
	v_pk_mul_f32 v[204:205], v[96:97], v[96:97]
	v_pk_mul_f32 v[206:207], v[94:95], v[94:95]
	v_lshl_add_u64 v[146:147], v[158:159], 0, s[10:11]
	global_store_dwordx4 v[146:147], v[150:153], off sc1
	v_mul_f32_e32 v146, v119, v119
	v_mul_f32_e32 v147, v121, v121
	v_fmac_f32_e32 v146, v118, v118
	v_fmac_f32_e32 v147, v120, v120
	v_add_f32_e32 v153, v146, v147
	v_pk_mul_f32 v[146:147], v[116:117], v[116:117]
	v_pk_mul_f32 v[148:149], v[114:115], v[114:115]
	v_bitop3_b32 v152, v199, s73, 16 bitop3:0xc8
	v_mov_b32_e32 v150, v146
	v_mov_b32_e32 v151, v148
	v_mov_b32_e32 v148, v147
	v_pk_add_f32 v[146:147], v[150:151], v[148:149]
	v_lshlrev_b32_e32 v170, 7, v152
	v_add_f32_e32 v147, v153, v147
	v_add_f32_e32 v210, v146, v147
	ds_read_b128 v[146:149], v245 offset:49152
	s_nop 0
	ds_read_b128 v[150:153], v244 offset:49152
	s_nop 0
	ds_read_b128 v[154:157], v245 offset:16384
	s_nop 0
	ds_read_b128 v[158:161], v244 offset:16384
	v_mov_b32_e32 v208, v204
	v_mov_b32_e32 v209, v206
	v_mov_b32_e32 v206, v205
	v_pk_add_f32 v[204:205], v[208:209], v[206:207]
	v_pk_mul_f32 v[206:207], v[90:91], v[90:91]
	v_add_f32_e32 v170, v210, v205
	v_add_f32_e32 v170, v204, v170
	v_pk_mul_f32 v[204:205], v[92:93], v[92:93]
	v_mov_b32_e32 v209, v206
	v_mov_b32_e32 v208, v204
	v_mov_b32_e32 v206, v205
	v_pk_add_f32 v[204:205], v[208:209], v[206:207]
	s_nop 0
	v_add_f32_e32 v170, v205, v170
	v_add_f32_e32 v170, v204, v170
	ds_bpermute_b32 v204, v201, v170
	s_waitcnt lgkmcnt(0)
	v_add_f32_e32 v170, v170, v204
	ds_bpermute_b32 v204, v202, v170
	s_waitcnt lgkmcnt(0)
	v_add_f32_e32 v170, v170, v204
	v_fmamk_f32 v170, v170, 0x3c800000, v195
	v_mul_f32_e32 v204, 0x4f800000, v170
	v_cmp_gt_f32_e32 vcc, s70, v170
	s_nop 1
	v_cndmask_b32_e32 v170, v170, v204, vcc
	v_sqrt_f32_e32 v204, v170
	s_nop 0
	v_add_u32_e32 v205, -1, v204
	v_fma_f32 v206, -v205, v204, v170
	v_cmp_ge_f32_e64 s[8:9], 0, v206
	v_add_u32_e32 v206, 1, v204
	s_nop 0
	v_cndmask_b32_e64 v205, v204, v205, s[8:9]
	v_fma_f32 v204, -v206, v204, v170
	v_cmp_lt_f32_e64 s[8:9], 0, v204
	s_nop 1
	v_cndmask_b32_e64 v204, v205, v206, s[8:9]
	v_mul_f32_e32 v205, 0x37800000, v204
	v_cndmask_b32_e32 v204, v204, v205, vcc
	v_cmp_class_f32_e32 vcc, v170, v196
	s_nop 1
	v_cndmask_b32_e32 v170, v204, v170, vcc
	v_div_scale_f32 v204, s[8:9], v170, v170, v200
	v_rcp_f32_e32 v205, v204
	s_mov_b64 s[8:9], -1
	v_fma_f32 v206, -v204, v205, 1.0
	v_fmac_f32_e32 v205, v206, v205
	v_div_scale_f32 v206, vcc, v200, v170, v200
	v_mul_f32_e32 v207, v206, v205
	v_fma_f32 v208, -v204, v207, v206
	v_fmac_f32_e32 v207, v208, v205
	v_fma_f32 v204, -v204, v207, v206
	v_div_fmas_f32 v204, v204, v205, v207
	v_div_fixup_f32 v170, v204, v170, v200
	v_pk_mul_f32 v[216:217], v[90:91], v[170:171] op_sel_hi:[1,0]
	v_pk_mul_f32 v[210:211], v[114:115], v[170:171] op_sel_hi:[1,0]
	v_pk_mul_f32 v[216:217], v[130:131], v[216:217]
	v_pk_mul_f32 v[210:211], v[138:139], v[210:211]
	v_pk_mul_f32 v[212:213], v[94:95], v[170:171] op_sel_hi:[1,0]
	v_pk_mul_f32 v[214:215], v[96:97], v[170:171] op_sel_hi:[1,0]
	s_waitcnt lgkmcnt(0)
	v_pk_mul_f32 v[224:225], v[146:147], v[216:217]
	v_pk_mul_f32 v[218:219], v[92:93], v[170:171] op_sel_hi:[1,0]
	s_waitcnt lgkmcnt(0)
	v_pk_fma_f32 v[224:225], v[154:155], v[210:211], v[224:225] neg_lo:[0,0,1] neg_hi:[0,0,1]
	v_pk_mul_f32 v[154:155], v[154:155], v[216:217]
	v_pk_mul_f32 v[204:205], v[120:121], v[170:171] op_sel_hi:[1,0]
	v_pk_fma_f32 v[154:155], v[146:147], v[210:211], v[154:155]
	v_lshlrev_b32_e32 v146, 3, v229
	v_pk_mul_f32 v[206:207], v[118:119], v[170:171] op_sel_hi:[1,0]
	v_pk_mul_f32 v[208:209], v[116:117], v[170:171] op_sel_hi:[1,0]
	v_pk_mul_f32 v[214:215], v[136:137], v[214:215]
	v_pk_mul_f32 v[212:213], v[134:135], v[212:213]
	v_pk_mul_f32 v[218:219], v[132:133], v[218:219]
	v_and_b32_e32 v146, 0xf8, v146
	v_pk_mul_f32 v[206:207], v[142:143], v[206:207]
	v_pk_mul_f32 v[204:205], v[144:145], v[204:205]
	v_pk_mul_f32 v[208:209], v[140:141], v[208:209]
	v_pk_mul_f32 v[220:221], v[150:151], v[212:213]
	v_pk_mul_f32 v[222:223], v[152:153], v[214:215]
	v_pk_mul_f32 v[226:227], v[148:149], v[218:219]
	v_or3_b32 v146, v228, v146, v184
	s_waitcnt lgkmcnt(0)
	v_pk_fma_f32 v[222:223], v[160:161], v[204:205], v[222:223] neg_lo:[0,0,1] neg_hi:[0,0,1]
	v_pk_fma_f32 v[220:221], v[158:159], v[206:207], v[220:221] neg_lo:[0,0,1] neg_hi:[0,0,1]
	v_pk_fma_f32 v[226:227], v[156:157], v[208:209], v[226:227] neg_lo:[0,0,1] neg_hi:[0,0,1]
	v_pk_mul_f32 v[158:159], v[158:159], v[212:213]
	v_pk_mul_f32 v[160:161], v[160:161], v[214:215]
	v_pk_mul_f32 v[156:157], v[156:157], v[218:219]
	v_ashrrev_i32_e32 v147, 31, v146
	v_pk_fma_f32 v[152:153], v[152:153], v[204:205], v[160:161]
	v_pk_fma_f32 v[150:151], v[150:151], v[206:207], v[158:159]
	v_pk_fma_f32 v[156:157], v[148:149], v[208:209], v[156:157]
	v_lshl_add_u64 v[158:159], v[146:147], 1, s[54:55]
	v_cvt_pk_f16_f32 v146, v220, v221
	v_cvt_pk_f16_f32 v147, v222, v223
	v_cvt_pk_f16_f32 v148, v224, v225
	v_cvt_pk_f16_f32 v149, v226, v227
	v_bitop3_b32 v184, v199, s74, 32 bitop3:0xc8
	v_cvt_pk_f16_f32 v150, v150, v151
	v_cvt_pk_f16_f32 v151, v152, v153
	v_cvt_pk_f16_f32 v152, v154, v155
	v_cvt_pk_f16_f32 v153, v156, v157
	global_store_dwordx4 v[158:159], v[146:149], off sc1
	v_lshlrev_b32_e32 v170, 7, v184
	v_mul_f32_e32 v204, v105, v105
	v_lshl_add_u64 v[146:147], v[158:159], 0, s[10:11]
	global_store_dwordx4 v[146:147], v[150:153], off sc1
	v_fmac_f32_e32 v204, v104, v104
	ds_read_b128 v[146:149], v245 offset:1024
	ds_read_b128 v[154:157], v244 offset:1024
	s_nop 0
	ds_read_b128 v[150:153], v245 offset:33792
	s_nop 0
	ds_read_b128 v[158:161], v244 offset:33792
	v_mul_f32_e32 v170, v103, v103
	v_fmac_f32_e32 v170, v102, v102
	v_add_f32_e32 v170, v170, v204
	v_pk_mul_f32 v[204:205], v[100:101], v[100:101]
	v_pk_mul_f32 v[206:207], v[98:99], v[98:99]
	v_mov_b32_e32 v208, v204
	v_mov_b32_e32 v209, v206
	v_mov_b32_e32 v206, v205
	v_pk_add_f32 v[204:205], v[208:209], v[206:207]
	v_pk_mul_f32 v[206:207], v[78:79], v[78:79]
	v_add_f32_e32 v170, v170, v205
	v_add_f32_e32 v170, v204, v170
	v_pk_mul_f32 v[204:205], v[80:81], v[80:81]
	v_mov_b32_e32 v209, v206
	v_mov_b32_e32 v208, v204
	v_mov_b32_e32 v206, v205
	v_pk_add_f32 v[204:205], v[208:209], v[206:207]
	v_pk_mul_f32 v[206:207], v[74:75], v[74:75]
	v_add_f32_e32 v170, v170, v205
	v_add_f32_e32 v170, v204, v170
	v_pk_mul_f32 v[204:205], v[76:77], v[76:77]
	v_mov_b32_e32 v209, v206
	v_mov_b32_e32 v208, v204
	v_mov_b32_e32 v206, v205
	v_pk_add_f32 v[204:205], v[208:209], v[206:207]
	s_mov_b64 vcc, s[4:5]
	v_add_f32_e32 v170, v205, v170
	v_add_f32_e32 v170, v204, v170
	ds_bpermute_b32 v204, v201, v170
	v_lshlrev_b32_e32 v205, 6, v184
	s_waitcnt lgkmcnt(0)
	v_add_f32_e32 v170, v170, v204
	ds_bpermute_b32 v204, v202, v170
	s_cbranch_vccnz .LBB1_17
	v_or_b32_e32 v184, 32, v199
	v_lshlrev_b32_e32 v184, 3, v184
	v_and_b32_e32 v206, 0x1f000, v205
	v_and_b32_e32 v184, 0x178, v184
	v_or3_b32 v184, v206, v184, v203
	s_mov_b64 s[8:9], 0

.LBB1_20:
	s_waitcnt lgkmcnt(0)
	v_add_f32_e32 v170, v170, v204
	v_fmamk_f32 v170, v170, 0x3c800000, v195
	v_mul_f32_e32 v185, 0x4f800000, v170
	v_cmp_gt_f32_e32 vcc, s70, v170
	s_lshl_b32 s10, s56, 1
	v_add_u32_e32 v228, 0x80, v199
	v_cndmask_b32_e32 v170, v170, v185, vcc
	v_sqrt_f32_e32 v185, v170
	s_nop 0
	v_add_u32_e32 v204, -1, v185
	v_fma_f32 v206, -v204, v185, v170
	v_add_u32_e32 v205, 1, v185
	v_cmp_ge_f32_e64 s[4:5], 0, v206
	s_nop 1
	v_cndmask_b32_e64 v204, v185, v204, s[4:5]
	v_fma_f32 v185, -v205, v185, v170
	v_cmp_lt_f32_e64 s[4:5], 0, v185
	s_nop 1
	v_cndmask_b32_e64 v185, v204, v205, s[4:5]
	v_mul_f32_e32 v204, 0x37800000, v185
	v_cndmask_b32_e32 v185, v185, v204, vcc
	v_cmp_class_f32_e32 vcc, v170, v196
	s_nop 1
	v_cndmask_b32_e32 v170, v185, v170, vcc
	v_div_scale_f32 v185, s[4:5], v170, v170, v200
	v_rcp_f32_e32 v204, v185
	s_nop 0
	v_fma_f32 v205, -v185, v204, 1.0
	v_fmac_f32_e32 v204, v205, v204
	v_div_scale_f32 v205, vcc, v200, v170, v200
	v_mul_f32_e32 v206, v205, v204
	v_fma_f32 v207, -v185, v206, v205
	v_fmac_f32_e32 v206, v207, v204
	v_fma_f32 v185, -v185, v206, v205
	v_div_fmas_f32 v185, v185, v204, v206
	v_div_fixup_f32 v170, v185, v170, v200
	v_pk_mul_f32 v[212:213], v[78:79], v[170:171] op_sel_hi:[1,0]
	v_pk_mul_f32 v[214:215], v[80:81], v[170:171] op_sel_hi:[1,0]
	v_pk_mul_f32 v[216:217], v[74:75], v[170:171] op_sel_hi:[1,0]
	v_pk_mul_f32 v[218:219], v[76:77], v[170:171] op_sel_hi:[1,0]
	v_pk_mul_f32 v[204:205], v[104:105], v[170:171] op_sel_hi:[1,0]
	v_pk_mul_f32 v[206:207], v[102:103], v[170:171] op_sel_hi:[1,0]
	v_pk_mul_f32 v[208:209], v[100:101], v[170:171] op_sel_hi:[1,0]
	v_pk_mul_f32 v[210:211], v[98:99], v[170:171] op_sel_hi:[1,0]
	v_pk_mul_f32 v[214:215], v[136:137], v[214:215]
	v_pk_mul_f32 v[212:213], v[134:135], v[212:213]
	v_pk_mul_f32 v[218:219], v[132:133], v[218:219]
	v_pk_mul_f32 v[216:217], v[130:131], v[216:217]
	v_pk_mul_f32 v[206:207], v[142:143], v[206:207]
	v_pk_mul_f32 v[204:205], v[144:145], v[204:205]
	v_pk_mul_f32 v[210:211], v[138:139], v[210:211]
	v_pk_mul_f32 v[208:209], v[140:141], v[208:209]
	s_waitcnt lgkmcnt(0)
	v_pk_mul_f32 v[220:221], v[158:159], v[212:213]
	v_pk_mul_f32 v[222:223], v[160:161], v[214:215]
	v_pk_mul_f32 v[224:225], v[150:151], v[216:217]
	v_pk_mul_f32 v[226:227], v[152:153], v[218:219]
	v_pk_fma_f32 v[222:223], v[156:157], v[204:205], v[222:223] neg_lo:[0,0,1] neg_hi:[0,0,1]
	v_pk_fma_f32 v[220:221], v[154:155], v[206:207], v[220:221] neg_lo:[0,0,1] neg_hi:[0,0,1]
	v_pk_fma_f32 v[226:227], v[148:149], v[208:209], v[226:227] neg_lo:[0,0,1] neg_hi:[0,0,1]
	v_pk_fma_f32 v[224:225], v[146:147], v[210:211], v[224:225] neg_lo:[0,0,1] neg_hi:[0,0,1]
	v_pk_mul_f32 v[154:155], v[154:155], v[212:213]
	v_pk_mul_f32 v[156:157], v[156:157], v[214:215]
	v_pk_mul_f32 v[146:147], v[146:147], v[216:217]
	v_pk_mul_f32 v[148:149], v[148:149], v[218:219]
	v_ashrrev_i32_e32 v185, 31, v184
	v_pk_fma_f32 v[156:157], v[160:161], v[204:205], v[156:157]
	v_pk_fma_f32 v[154:155], v[158:159], v[206:207], v[154:155]
	v_pk_fma_f32 v[158:159], v[152:153], v[208:209], v[148:149]
	v_pk_fma_f32 v[152:153], v[150:151], v[210:211], v[146:147]
	v_lshl_add_u64 v[160:161], v[184:185], 1, s[8:9]
	v_cvt_pk_f16_f32 v146, v220, v221
	v_cvt_pk_f16_f32 v147, v222, v223
	v_cvt_pk_f16_f32 v148, v224, v225
	v_cvt_pk_f16_f32 v149, v226, v227
	v_cvt_pk_f16_f32 v150, v154, v155
	v_cvt_pk_f16_f32 v151, v156, v157
	v_cvt_pk_f16_f32 v152, v152, v153
	v_cvt_pk_f16_f32 v153, v158, v159
	global_store_dwordx4 v[160:161], v[146:149], off sc1
	v_bitop3_b32 v226, v199, s75, 48 bitop3:0xc8
	v_lshlrev_b32_e32 v170, 7, v226
	v_lshl_add_u64 v[146:147], v[160:161], 0, s[10:11]
	global_store_dwordx4 v[146:147], v[150:153], off sc1
	v_mul_f32_e32 v146, v87, v87
	v_mul_f32_e32 v147, v89, v89
	v_fmac_f32_e32 v146, v86, v86
	v_fmac_f32_e32 v147, v88, v88
	v_add_f32_e32 v152, v146, v147
	v_pk_mul_f32 v[146:147], v[84:85], v[84:85]
	v_pk_mul_f32 v[148:149], v[82:83], v[82:83]
	v_mov_b32_e32 v150, v146
	v_mov_b32_e32 v151, v148
	v_mov_b32_e32 v148, v147
	v_pk_add_f32 v[146:147], v[150:151], v[148:149]
	v_add_f32_e32 v147, v152, v147
	v_add_f32_e32 v208, v146, v147
	ds_read_b128 v[146:149], v245 offset:50176
	s_nop 0
	ds_read_b128 v[150:153], v244 offset:50176
	s_nop 0
	ds_read_b128 v[154:157], v245 offset:17408
	s_nop 0
	ds_read_b128 v[158:161], v244 offset:17408
	v_pk_mul_f32 v[184:185], v[72:73], v[72:73]
	v_pk_mul_f32 v[204:205], v[70:71], v[70:71]
	v_mov_b32_e32 v206, v184
	v_mov_b32_e32 v207, v204
	v_mov_b32_e32 v204, v185
	v_pk_add_f32 v[184:185], v[206:207], v[204:205]
	v_pk_mul_f32 v[204:205], v[66:67], v[66:67]
	v_add_f32_e32 v170, v208, v185
	v_add_f32_e32 v170, v184, v170
	v_pk_mul_f32 v[184:185], v[68:69], v[68:69]
	v_mov_b32_e32 v207, v204
	v_mov_b32_e32 v206, v184
	v_mov_b32_e32 v204, v185
	v_pk_add_f32 v[184:185], v[206:207], v[204:205]
	v_or_b32_e32 v227, 48, v199
	v_add_f32_e32 v170, v185, v170
	v_add_f32_e32 v170, v184, v170
	ds_bpermute_b32 v184, v201, v170
	s_waitcnt lgkmcnt(0)
	v_add_f32_e32 v170, v170, v184
	ds_bpermute_b32 v184, v202, v170
	s_waitcnt lgkmcnt(0)
	v_add_f32_e32 v170, v170, v184
	v_fmamk_f32 v170, v170, 0x3c800000, v195
	v_mul_f32_e32 v184, 0x4f800000, v170
	v_cmp_gt_f32_e32 vcc, s70, v170
	s_nop 1
	v_cndmask_b32_e32 v170, v170, v184, vcc
	v_sqrt_f32_e32 v184, v170
	s_nop 0
	v_add_u32_e32 v185, -1, v184
	v_fma_f32 v204, -v185, v184, v170
	v_cmp_ge_f32_e64 s[4:5], 0, v204
	v_add_u32_e32 v204, 1, v184
	s_nop 0
	v_cndmask_b32_e64 v185, v184, v185, s[4:5]
	v_fma_f32 v184, -v204, v184, v170
	v_cmp_lt_f32_e64 s[4:5], 0, v184
	s_nop 1
	v_cndmask_b32_e64 v184, v185, v204, s[4:5]
	v_mul_f32_e32 v185, 0x37800000, v184
	v_cndmask_b32_e32 v184, v184, v185, vcc
	v_cmp_class_f32_e32 vcc, v170, v196
	s_nop 1
	v_cndmask_b32_e32 v170, v184, v170, vcc
	v_div_scale_f32 v184, s[4:5], v170, v170, v200
	v_rcp_f32_e32 v185, v184
	s_nop 0
	v_fma_f32 v204, -v184, v185, 1.0
	v_fmac_f32_e32 v185, v204, v185
	v_div_scale_f32 v204, vcc, v200, v170, v200
	v_mul_f32_e32 v205, v204, v185
	v_fma_f32 v206, -v184, v205, v204
	v_fmac_f32_e32 v205, v206, v185
	v_fma_f32 v184, -v184, v205, v204
	v_div_fmas_f32 v184, v184, v185, v205
	v_div_fixup_f32 v170, v184, v170, v200
	v_pk_mul_f32 v[214:215], v[66:67], v[170:171] op_sel_hi:[1,0]
	v_pk_mul_f32 v[208:209], v[82:83], v[170:171] op_sel_hi:[1,0]
	v_pk_mul_f32 v[214:215], v[130:131], v[214:215]
	v_pk_mul_f32 v[208:209], v[138:139], v[208:209]
	s_waitcnt lgkmcnt(0)
	v_pk_mul_f32 v[222:223], v[146:147], v[214:215]
	v_pk_mul_f32 v[210:211], v[70:71], v[170:171] op_sel_hi:[1,0]
	s_waitcnt lgkmcnt(0)
	v_pk_fma_f32 v[222:223], v[154:155], v[208:209], v[222:223] neg_lo:[0,0,1] neg_hi:[0,0,1]
	v_pk_mul_f32 v[154:155], v[154:155], v[214:215]
	v_pk_mul_f32 v[212:213], v[72:73], v[170:171] op_sel_hi:[1,0]
	v_pk_mul_f32 v[216:217], v[68:69], v[170:171] op_sel_hi:[1,0]
	v_pk_fma_f32 v[154:155], v[146:147], v[208:209], v[154:155]
	v_lshlrev_b32_e32 v146, 6, v226
	v_lshlrev_b32_e32 v147, 3, v227
	v_pk_mul_f32 v[184:185], v[88:89], v[170:171] op_sel_hi:[1,0]
	v_pk_mul_f32 v[204:205], v[86:87], v[170:171] op_sel_hi:[1,0]
	v_pk_mul_f32 v[206:207], v[84:85], v[170:171] op_sel_hi:[1,0]
	v_pk_mul_f32 v[212:213], v[136:137], v[212:213]
	v_pk_mul_f32 v[210:211], v[134:135], v[210:211]
	v_pk_mul_f32 v[216:217], v[132:133], v[216:217]
	v_and_b32_e32 v146, s79, v146
	v_and_b32_e32 v147, s57, v147
	v_pk_mul_f32 v[204:205], v[142:143], v[204:205]
	v_pk_mul_f32 v[184:185], v[144:145], v[184:185]
	v_pk_mul_f32 v[206:207], v[140:141], v[206:207]
	v_pk_mul_f32 v[218:219], v[150:151], v[210:211]
	v_pk_mul_f32 v[220:221], v[152:153], v[212:213]
	v_pk_mul_f32 v[224:225], v[148:149], v[216:217]
	v_or3_b32 v146, v147, v203, v146
	s_waitcnt lgkmcnt(0)
	v_pk_fma_f32 v[220:221], v[160:161], v[184:185], v[220:221] neg_lo:[0,0,1] neg_hi:[0,0,1]
	v_pk_fma_f32 v[218:219], v[158:159], v[204:205], v[218:219] neg_lo:[0,0,1] neg_hi:[0,0,1]
	v_pk_fma_f32 v[224:225], v[156:157], v[206:207], v[224:225] neg_lo:[0,0,1] neg_hi:[0,0,1]
	v_pk_mul_f32 v[158:159], v[158:159], v[210:211]
	v_pk_mul_f32 v[160:161], v[160:161], v[212:213]
	v_pk_mul_f32 v[156:157], v[156:157], v[216:217]
	v_ashrrev_i32_e32 v147, 31, v146
	v_pk_fma_f32 v[152:153], v[152:153], v[184:185], v[160:161]
	v_pk_fma_f32 v[150:151], v[150:151], v[204:205], v[158:159]
	v_pk_fma_f32 v[156:157], v[148:149], v[206:207], v[156:157]
	v_lshl_add_u64 v[158:159], v[146:147], 1, s[8:9]
	v_cvt_pk_f16_f32 v146, v218, v219
	v_cvt_pk_f16_f32 v147, v220, v221
	v_cvt_pk_f16_f32 v148, v222, v223
	v_cvt_pk_f16_f32 v149, v224, v225
	v_cvt_pk_f16_f32 v150, v150, v151
	v_cvt_pk_f16_f32 v151, v152, v153
	v_cvt_pk_f16_f32 v152, v154, v155
	v_cvt_pk_f16_f32 v153, v156, v157
	global_store_dwordx4 v[158:159], v[146:149], off sc1
	v_pk_mul_f32 v[184:185], v[48:49], v[48:49]
	v_pk_mul_f32 v[204:205], v[46:47], v[46:47]
	v_lshl_add_u64 v[146:147], v[158:159], 0, s[10:11]
	global_store_dwordx4 v[146:147], v[150:153], off sc1
	v_mul_f32_e32 v146, v63, v63
	v_mul_f32_e32 v147, v65, v65
	v_fmac_f32_e32 v146, v62, v62
	v_fmac_f32_e32 v147, v64, v64
	v_add_f32_e32 v153, v146, v147
	v_pk_mul_f32 v[146:147], v[60:61], v[60:61]
	v_pk_mul_f32 v[148:149], v[58:59], v[58:59]
	v_and_b32_e32 v152, 0x7cf, v228
	v_mov_b32_e32 v150, v146
	v_mov_b32_e32 v151, v148
	v_mov_b32_e32 v148, v147
	v_pk_add_f32 v[146:147], v[150:151], v[148:149]
	v_lshlrev_b32_e32 v170, 7, v152
	v_add_f32_e32 v147, v153, v147
	v_add_f32_e32 v203, v146, v147
	ds_read_b128 v[146:149], v245 offset:34816
	s_nop 0
	ds_read_b128 v[150:153], v244 offset:34816
	s_nop 0
	ds_read_b128 v[154:157], v245 offset:2048
	s_nop 0
	ds_read_b128 v[158:161], v244 offset:2048
	v_mov_b32_e32 v206, v184
	v_mov_b32_e32 v207, v204
	v_mov_b32_e32 v204, v185
	v_pk_add_f32 v[184:185], v[206:207], v[204:205]
	v_pk_mul_f32 v[204:205], v[42:43], v[42:43]
	v_add_f32_e32 v170, v203, v185
	v_add_f32_e32 v170, v184, v170
	v_pk_mul_f32 v[184:185], v[44:45], v[44:45]
	v_mov_b32_e32 v207, v204
	v_mov_b32_e32 v206, v184
	v_mov_b32_e32 v204, v185
	v_pk_add_f32 v[184:185], v[206:207], v[204:205]
	s_nop 0
	v_add_f32_e32 v170, v185, v170
	v_add_f32_e32 v170, v184, v170
	ds_bpermute_b32 v184, v201, v170
	v_lshrrev_b32_e32 v185, 8, v228
	v_and_b32_e32 v185, 0x7ff8, v185
	v_add_u32_e32 v185, s78, v185
	v_lshl_or_b32 v203, v185, 17, v187
	s_waitcnt lgkmcnt(0)
	v_add_f32_e32 v170, v170, v184
	ds_bpermute_b32 v184, v202, v170
	v_lshrrev_b32_e32 v185, 6, v228
	v_and_b32_e32 v185, 0x7fe0, v185
	v_add_u32_e32 v185, s37, v185
	v_lshl_or_b32 v185, v185, 17, v188
	s_waitcnt lgkmcnt(0)
	v_add_f32_e32 v170, v170, v184
	v_fmamk_f32 v170, v170, 0x3c800000, v195
	v_mul_f32_e32 v184, 0x4f800000, v170
	v_cmp_gt_f32_e32 vcc, s70, v170
	s_nop 1
	v_cndmask_b32_e32 v170, v170, v184, vcc
	v_sqrt_f32_e32 v184, v170
	s_nop 0
	v_add_u32_e32 v204, -1, v184
	v_fma_f32 v205, -v204, v184, v170
	v_cmp_ge_f32_e64 s[4:5], 0, v205
	v_add_u32_e32 v205, 1, v184
	s_nop 0
	v_cndmask_b32_e64 v204, v184, v204, s[4:5]
	v_fma_f32 v184, -v205, v184, v170
	v_cmp_lt_f32_e64 s[4:5], 0, v184
	s_nop 1
	v_cndmask_b32_e64 v184, v204, v205, s[4:5]
	v_mul_f32_e32 v204, 0x37800000, v184
	v_cndmask_b32_e32 v184, v184, v204, vcc
	v_cmp_class_f32_e32 vcc, v170, v196
	s_nop 1
	v_cndmask_b32_e32 v170, v184, v170, vcc
	v_div_scale_f32 v184, s[4:5], v170, v170, v200
	v_rcp_f32_e32 v204, v184
	s_nop 0
	v_fma_f32 v205, -v184, v204, 1.0
	v_fmac_f32_e32 v204, v205, v204
	v_div_scale_f32 v205, vcc, v200, v170, v200
	v_mul_f32_e32 v206, v205, v204
	v_fma_f32 v207, -v184, v206, v205
	v_fmac_f32_e32 v206, v207, v204
	v_fma_f32 v184, -v184, v206, v205
	v_div_fmas_f32 v184, v184, v204, v206
	v_div_fixup_f32 v170, v184, v170, v200
	v_pk_mul_f32 v[216:217], v[42:43], v[170:171] op_sel_hi:[1,0]
	v_pk_mul_f32 v[210:211], v[58:59], v[170:171] op_sel_hi:[1,0]
	v_pk_mul_f32 v[216:217], v[130:131], v[216:217]
	v_pk_mul_f32 v[210:211], v[138:139], v[210:211]
	v_pk_mul_f32 v[212:213], v[46:47], v[170:171] op_sel_hi:[1,0]
	v_pk_mul_f32 v[214:215], v[48:49], v[170:171] op_sel_hi:[1,0]
	s_waitcnt lgkmcnt(0)
	v_pk_mul_f32 v[224:225], v[146:147], v[216:217]
	v_pk_mul_f32 v[218:219], v[44:45], v[170:171] op_sel_hi:[1,0]
	s_waitcnt lgkmcnt(0)
	v_pk_fma_f32 v[224:225], v[154:155], v[210:211], v[224:225] neg_lo:[0,0,1] neg_hi:[0,0,1]
	v_pk_mul_f32 v[154:155], v[154:155], v[216:217]
	v_pk_mul_f32 v[204:205], v[64:65], v[170:171] op_sel_hi:[1,0]
	v_pk_fma_f32 v[154:155], v[146:147], v[210:211], v[154:155]
	v_lshlrev_b32_e32 v146, 6, v228
	v_pk_mul_f32 v[206:207], v[62:63], v[170:171] op_sel_hi:[1,0]
	v_pk_mul_f32 v[208:209], v[60:61], v[170:171] op_sel_hi:[1,0]
	v_pk_mul_f32 v[214:215], v[136:137], v[214:215]
	v_pk_mul_f32 v[212:213], v[134:135], v[212:213]
	v_pk_mul_f32 v[218:219], v[132:133], v[218:219]
	v_cndmask_b32_e64 v184, v203, v185, s[6:7]
	v_and_b32_e32 v146, 0x1f000, v146
	v_pk_mul_f32 v[206:207], v[142:143], v[206:207]
	v_pk_mul_f32 v[204:205], v[144:145], v[204:205]
	v_pk_mul_f32 v[208:209], v[140:141], v[208:209]
	v_pk_mul_f32 v[220:221], v[150:151], v[212:213]
	v_pk_mul_f32 v[222:223], v[152:153], v[214:215]
	v_pk_mul_f32 v[226:227], v[148:149], v[218:219]
	v_or3_b32 v146, v146, v189, v184
	s_waitcnt lgkmcnt(0)
	v_pk_fma_f32 v[222:223], v[160:161], v[204:205], v[222:223] neg_lo:[0,0,1] neg_hi:[0,0,1]
	v_pk_fma_f32 v[220:221], v[158:159], v[206:207], v[220:221] neg_lo:[0,0,1] neg_hi:[0,0,1]
	v_pk_fma_f32 v[226:227], v[156:157], v[208:209], v[226:227] neg_lo:[0,0,1] neg_hi:[0,0,1]
	v_pk_mul_f32 v[158:159], v[158:159], v[212:213]
	v_pk_mul_f32 v[160:161], v[160:161], v[214:215]
	v_pk_mul_f32 v[156:157], v[156:157], v[218:219]
	v_ashrrev_i32_e32 v147, 31, v146
	v_pk_fma_f32 v[152:153], v[152:153], v[204:205], v[160:161]
	v_pk_fma_f32 v[150:151], v[150:151], v[206:207], v[158:159]
	v_pk_fma_f32 v[156:157], v[148:149], v[208:209], v[156:157]
	v_lshl_add_u64 v[158:159], v[146:147], 1, s[54:55]
	v_cvt_pk_f16_f32 v146, v220, v221
	v_cvt_pk_f16_f32 v147, v222, v223
	v_cvt_pk_f16_f32 v148, v224, v225
	v_cvt_pk_f16_f32 v149, v226, v227
	v_cvt_pk_f16_f32 v150, v150, v151
	v_cvt_pk_f16_f32 v151, v152, v153
	v_cvt_pk_f16_f32 v152, v154, v155
	v_cvt_pk_f16_f32 v153, v156, v157
	global_store_dwordx4 v[158:159], v[146:149], off sc1
	v_add_u32_e32 v228, 0x90, v199
	v_pk_mul_f32 v[204:205], v[32:33], v[32:33]
	v_lshl_add_u64 v[146:147], v[158:159], 0, s[10:11]
	global_store_dwordx4 v[146:147], v[150:153], off sc1
	v_mul_f32_e32 v146, v55, v55
	v_mul_f32_e32 v147, v57, v57
	v_fmac_f32_e32 v146, v54, v54
	v_fmac_f32_e32 v147, v56, v56
	v_add_f32_e32 v153, v146, v147
	v_pk_mul_f32 v[146:147], v[52:53], v[52:53]
	v_pk_mul_f32 v[148:149], v[50:51], v[50:51]
	v_and_b32_e32 v152, 0x7df, v228
	v_mov_b32_e32 v150, v146
	v_mov_b32_e32 v151, v148
	v_mov_b32_e32 v148, v147
	v_pk_add_f32 v[146:147], v[150:151], v[148:149]
	v_lshlrev_b32_e32 v170, 7, v152
	v_add_f32_e32 v147, v153, v147
	v_add_f32_e32 v210, v146, v147
	ds_read_b128 v[146:149], v245 offset:51200
	s_nop 0
	ds_read_b128 v[150:153], v244 offset:51200
	s_nop 0
	ds_read_b128 v[154:157], v245 offset:18432
	s_nop 0
	ds_read_b128 v[158:161], v244 offset:18432
	v_pk_mul_f32 v[206:207], v[30:31], v[30:31]
	v_mov_b32_e32 v208, v204
	v_mov_b32_e32 v209, v206
	v_mov_b32_e32 v206, v205
	v_pk_add_f32 v[204:205], v[208:209], v[206:207]
	v_pk_mul_f32 v[206:207], v[26:27], v[26:27]
	v_add_f32_e32 v170, v210, v205
	v_add_f32_e32 v170, v204, v170
	v_pk_mul_f32 v[204:205], v[28:29], v[28:29]
	v_mov_b32_e32 v209, v206
	v_mov_b32_e32 v208, v204
	v_mov_b32_e32 v206, v205
	v_pk_add_f32 v[204:205], v[208:209], v[206:207]
	s_nop 0
	v_add_f32_e32 v170, v205, v170
	v_add_f32_e32 v170, v204, v170
	ds_bpermute_b32 v204, v201, v170
	s_waitcnt lgkmcnt(0)
	v_add_f32_e32 v170, v170, v204
	ds_bpermute_b32 v204, v202, v170
	s_waitcnt lgkmcnt(0)
	v_add_f32_e32 v170, v170, v204
	v_fmamk_f32 v170, v170, 0x3c800000, v195
	v_mul_f32_e32 v204, 0x4f800000, v170
	v_cmp_gt_f32_e32 vcc, s70, v170
	s_nop 1
	v_cndmask_b32_e32 v170, v170, v204, vcc
	v_sqrt_f32_e32 v204, v170
	s_nop 0
	v_add_u32_e32 v205, -1, v204
	v_fma_f32 v206, -v205, v204, v170
	v_cmp_ge_f32_e64 s[4:5], 0, v206
	v_add_u32_e32 v206, 1, v204
	s_nop 0
	v_cndmask_b32_e64 v205, v204, v205, s[4:5]
	v_fma_f32 v204, -v206, v204, v170
	v_cmp_lt_f32_e64 s[4:5], 0, v204
	s_nop 1
	v_cndmask_b32_e64 v204, v205, v206, s[4:5]
	v_mul_f32_e32 v205, 0x37800000, v204
	v_cndmask_b32_e32 v204, v204, v205, vcc
	v_cmp_class_f32_e32 vcc, v170, v196
	s_nop 1
	v_cndmask_b32_e32 v170, v204, v170, vcc
	v_div_scale_f32 v204, s[4:5], v170, v170, v200
	v_rcp_f32_e32 v205, v204
	s_mov_b64 s[4:5], -1
	v_fma_f32 v206, -v204, v205, 1.0
	v_fmac_f32_e32 v205, v206, v205
	v_div_scale_f32 v206, vcc, v200, v170, v200
	v_mul_f32_e32 v207, v206, v205
	v_fma_f32 v208, -v204, v207, v206
	v_fmac_f32_e32 v207, v208, v205
	v_fma_f32 v204, -v204, v207, v206
	v_div_fmas_f32 v204, v204, v205, v207
	v_div_fixup_f32 v170, v204, v170, v200
	v_pk_mul_f32 v[216:217], v[26:27], v[170:171] op_sel_hi:[1,0]
	v_pk_mul_f32 v[210:211], v[50:51], v[170:171] op_sel_hi:[1,0]
	v_pk_mul_f32 v[216:217], v[130:131], v[216:217]
	v_pk_mul_f32 v[210:211], v[138:139], v[210:211]
	v_pk_mul_f32 v[214:215], v[32:33], v[170:171] op_sel_hi:[1,0]
	s_waitcnt lgkmcnt(0)
	v_pk_mul_f32 v[224:225], v[146:147], v[216:217]
	v_pk_mul_f32 v[204:205], v[56:57], v[170:171] op_sel_hi:[1,0]
	s_waitcnt lgkmcnt(0)
	v_pk_fma_f32 v[224:225], v[154:155], v[210:211], v[224:225] neg_lo:[0,0,1] neg_hi:[0,0,1]
	v_pk_mul_f32 v[154:155], v[154:155], v[216:217]
	v_pk_mul_f32 v[212:213], v[30:31], v[170:171] op_sel_hi:[1,0]
	v_pk_mul_f32 v[214:215], v[136:137], v[214:215]
	v_pk_mul_f32 v[218:219], v[28:29], v[170:171] op_sel_hi:[1,0]
	v_pk_fma_f32 v[154:155], v[146:147], v[210:211], v[154:155]
	v_lshlrev_b32_e32 v146, 6, v228
	v_lshlrev_b32_e32 v147, 3, v228
	v_pk_mul_f32 v[206:207], v[54:55], v[170:171] op_sel_hi:[1,0]
	v_pk_mul_f32 v[204:205], v[144:145], v[204:205]
	v_pk_mul_f32 v[208:209], v[52:53], v[170:171] op_sel_hi:[1,0]
	v_pk_mul_f32 v[212:213], v[134:135], v[212:213]
	v_pk_mul_f32 v[218:219], v[132:133], v[218:219]
	v_pk_mul_f32 v[222:223], v[152:153], v[214:215]
	v_and_b32_e32 v146, 0x1f000, v146
	v_and_b32_e32 v147, 0xf8, v147
	v_pk_mul_f32 v[206:207], v[142:143], v[206:207]
	v_pk_mul_f32 v[208:209], v[140:141], v[208:209]
	v_pk_mul_f32 v[220:221], v[150:151], v[212:213]
	s_waitcnt lgkmcnt(0)
	v_pk_fma_f32 v[222:223], v[160:161], v[204:205], v[222:223] neg_lo:[0,0,1] neg_hi:[0,0,1]
	v_pk_mul_f32 v[226:227], v[148:149], v[218:219]
	v_pk_mul_f32 v[160:161], v[160:161], v[214:215]
	v_or3_b32 v146, v146, v147, v184
	v_pk_fma_f32 v[220:221], v[158:159], v[206:207], v[220:221] neg_lo:[0,0,1] neg_hi:[0,0,1]
	v_pk_fma_f32 v[226:227], v[156:157], v[208:209], v[226:227] neg_lo:[0,0,1] neg_hi:[0,0,1]
	v_pk_mul_f32 v[158:159], v[158:159], v[212:213]
	v_pk_fma_f32 v[152:153], v[152:153], v[204:205], v[160:161]
	v_pk_mul_f32 v[156:157], v[156:157], v[218:219]
	v_ashrrev_i32_e32 v147, 31, v146
	v_add_u32_e32 v204, 0xa0, v199
	v_pk_fma_f32 v[150:151], v[150:151], v[206:207], v[158:159]
	v_pk_fma_f32 v[156:157], v[148:149], v[208:209], v[156:157]
	v_lshl_add_u64 v[158:159], v[146:147], 1, s[54:55]
	v_cvt_pk_f16_f32 v146, v220, v221
	v_cvt_pk_f16_f32 v147, v222, v223
	v_cvt_pk_f16_f32 v148, v224, v225
	v_cvt_pk_f16_f32 v149, v226, v227
	v_and_b32_e32 v184, 0x7ef, v204
	v_cvt_pk_f16_f32 v150, v150, v151
	v_cvt_pk_f16_f32 v151, v152, v153
	v_cvt_pk_f16_f32 v152, v154, v155
	v_cvt_pk_f16_f32 v153, v156, v157
	global_store_dwordx4 v[158:159], v[146:149], off sc1
	v_lshlrev_b32_e32 v170, 7, v184
	v_mul_f32_e32 v205, v41, v41
	v_lshl_add_u64 v[146:147], v[158:159], 0, s[10:11]
	global_store_dwordx4 v[146:147], v[150:153], off sc1
	v_pk_mul_f32 v[206:207], v[36:37], v[36:37]
	ds_read_b128 v[146:149], v245 offset:3072
	ds_read_b128 v[154:157], v244 offset:3072
	s_nop 0
	ds_read_b128 v[150:153], v245 offset:35840
	s_nop 0
	ds_read_b128 v[158:161], v244 offset:35840
	v_mul_f32_e32 v170, v39, v39
	v_pk_mul_f32 v[208:209], v[34:35], v[34:35]
	v_fmac_f32_e32 v170, v38, v38
	v_fmac_f32_e32 v205, v40, v40
	v_mov_b32_e32 v210, v206
	v_mov_b32_e32 v211, v208
	v_mov_b32_e32 v208, v207
	v_add_f32_e32 v170, v170, v205
	v_pk_add_f32 v[206:207], v[210:211], v[208:209]
	v_pk_mul_f32 v[208:209], v[14:15], v[14:15]
	v_add_f32_e32 v170, v170, v207
	v_add_f32_e32 v170, v206, v170
	v_pk_mul_f32 v[206:207], v[16:17], v[16:17]
	v_mov_b32_e32 v211, v208
	v_mov_b32_e32 v210, v206
	v_mov_b32_e32 v208, v207
	v_pk_add_f32 v[206:207], v[210:211], v[208:209]
	v_pk_mul_f32 v[208:209], v[10:11], v[10:11]
	v_add_f32_e32 v170, v170, v207
	v_add_f32_e32 v170, v206, v170
	v_pk_mul_f32 v[206:207], v[12:13], v[12:13]
	v_mov_b32_e32 v211, v208
	v_mov_b32_e32 v210, v206
	v_mov_b32_e32 v208, v207
	v_pk_add_f32 v[206:207], v[210:211], v[208:209]
	s_andn2_b64 vcc, exec, s[52:53]
	v_add_f32_e32 v170, v207, v170
	v_add_f32_e32 v170, v206, v170
	ds_bpermute_b32 v205, v201, v170
	v_lshlrev_b32_e32 v206, 6, v184
	s_waitcnt lgkmcnt(0)
	v_add_f32_e32 v170, v170, v205
	ds_bpermute_b32 v205, v202, v170
	s_cbranch_vccnz .LBB1_22
	v_lshlrev_b32_e32 v204, 3, v204
	v_and_b32_e32 v184, 0x1f000, v206
	v_and_b32_e32 v204, 0x178, v204
	v_or3_b32 v184, v184, v204, v203
	s_mov_b64 s[4:5], 0

.LBB1_25:
	s_waitcnt lgkmcnt(0)
	v_add_f32_e32 v170, v170, v205
	v_fmamk_f32 v170, v170, 0x3c800000, v195
	v_mul_f32_e32 v185, 0x4f800000, v170
	v_cmp_gt_f32_e32 vcc, s70, v170
	s_lshl_b32 s10, s8, 1
	s_nop 0
	v_cndmask_b32_e32 v170, v170, v185, vcc
	v_sqrt_f32_e32 v185, v170
	s_nop 0
	v_add_u32_e32 v204, -1, v185
	v_fma_f32 v206, -v204, v185, v170
	v_add_u32_e32 v205, 1, v185
	v_cmp_ge_f32_e64 s[4:5], 0, v206
	s_nop 1
	v_cndmask_b32_e64 v204, v185, v204, s[4:5]
	v_fma_f32 v185, -v205, v185, v170
	v_cmp_lt_f32_e64 s[4:5], 0, v185
	s_nop 1
	v_cndmask_b32_e64 v185, v204, v205, s[4:5]
	v_mul_f32_e32 v204, 0x37800000, v185
	v_cndmask_b32_e32 v185, v185, v204, vcc
	v_cmp_class_f32_e32 vcc, v170, v196
	s_nop 1
	v_cndmask_b32_e32 v170, v185, v170, vcc
	v_div_scale_f32 v185, s[4:5], v170, v170, v200
	v_rcp_f32_e32 v204, v185
	s_nop 0
	v_fma_f32 v205, -v185, v204, 1.0
	v_fmac_f32_e32 v204, v205, v204
	v_div_scale_f32 v205, vcc, v200, v170, v200
	v_mul_f32_e32 v206, v205, v204
	v_fma_f32 v207, -v185, v206, v205
	v_fmac_f32_e32 v206, v207, v204
	v_fma_f32 v185, -v185, v206, v205
	v_div_fmas_f32 v185, v185, v204, v206
	v_div_fixup_f32 v170, v185, v170, v200
	v_pk_mul_f32 v[212:213], v[14:15], v[170:171] op_sel_hi:[1,0]
	v_pk_mul_f32 v[214:215], v[16:17], v[170:171] op_sel_hi:[1,0]
	v_pk_mul_f32 v[216:217], v[10:11], v[170:171] op_sel_hi:[1,0]
	v_pk_mul_f32 v[218:219], v[12:13], v[170:171] op_sel_hi:[1,0]
	v_pk_mul_f32 v[204:205], v[40:41], v[170:171] op_sel_hi:[1,0]
	v_pk_mul_f32 v[206:207], v[38:39], v[170:171] op_sel_hi:[1,0]
	v_pk_mul_f32 v[208:209], v[36:37], v[170:171] op_sel_hi:[1,0]
	v_pk_mul_f32 v[210:211], v[34:35], v[170:171] op_sel_hi:[1,0]
	v_pk_mul_f32 v[214:215], v[136:137], v[214:215]
	v_pk_mul_f32 v[212:213], v[134:135], v[212:213]
	v_pk_mul_f32 v[218:219], v[132:133], v[218:219]
	v_pk_mul_f32 v[216:217], v[130:131], v[216:217]
	v_pk_mul_f32 v[206:207], v[142:143], v[206:207]
	v_pk_mul_f32 v[204:205], v[144:145], v[204:205]
	v_pk_mul_f32 v[210:211], v[138:139], v[210:211]
	v_pk_mul_f32 v[208:209], v[140:141], v[208:209]
	s_waitcnt lgkmcnt(0)
	v_pk_mul_f32 v[220:221], v[158:159], v[212:213]
	v_pk_mul_f32 v[222:223], v[160:161], v[214:215]
	v_pk_mul_f32 v[224:225], v[150:151], v[216:217]
	v_pk_mul_f32 v[226:227], v[152:153], v[218:219]
	v_pk_fma_f32 v[222:223], v[156:157], v[204:205], v[222:223] neg_lo:[0,0,1] neg_hi:[0,0,1]
	v_pk_fma_f32 v[220:221], v[154:155], v[206:207], v[220:221] neg_lo:[0,0,1] neg_hi:[0,0,1]
	v_pk_fma_f32 v[226:227], v[148:149], v[208:209], v[226:227] neg_lo:[0,0,1] neg_hi:[0,0,1]
	v_pk_fma_f32 v[224:225], v[146:147], v[210:211], v[224:225] neg_lo:[0,0,1] neg_hi:[0,0,1]
	v_pk_mul_f32 v[154:155], v[154:155], v[212:213]
	v_pk_mul_f32 v[156:157], v[156:157], v[214:215]
	v_pk_mul_f32 v[146:147], v[146:147], v[216:217]
	v_pk_mul_f32 v[148:149], v[148:149], v[218:219]
	v_ashrrev_i32_e32 v185, 31, v184
	v_pk_fma_f32 v[156:157], v[160:161], v[204:205], v[156:157]
	v_pk_fma_f32 v[154:155], v[158:159], v[206:207], v[154:155]
	v_pk_fma_f32 v[158:159], v[152:153], v[208:209], v[148:149]
	v_pk_fma_f32 v[152:153], v[150:151], v[210:211], v[146:147]
	v_lshl_add_u64 v[160:161], v[184:185], 1, s[6:7]
	v_cvt_pk_f16_f32 v146, v220, v221
	v_cvt_pk_f16_f32 v147, v222, v223
	v_cvt_pk_f16_f32 v148, v224, v225
	v_cvt_pk_f16_f32 v149, v226, v227
	v_cvt_pk_f16_f32 v150, v154, v155
	v_cvt_pk_f16_f32 v151, v156, v157
	v_cvt_pk_f16_f32 v152, v152, v153
	v_cvt_pk_f16_f32 v153, v158, v159
	global_store_dwordx4 v[160:161], v[146:149], off sc1
	v_add_u32_e32 v208, 0xb0, v199
	v_and_b32_e32 v209, 0x7ff, v208
	v_lshl_add_u64 v[146:147], v[160:161], 0, s[10:11]
	global_store_dwordx4 v[146:147], v[150:153], off sc1
	v_mul_f32_e32 v146, v23, v23
	v_mul_f32_e32 v147, v25, v25
	v_fmac_f32_e32 v146, v22, v22
	v_fmac_f32_e32 v147, v24, v24
	v_add_f32_e32 v152, v146, v147
	v_pk_mul_f32 v[146:147], v[20:21], v[20:21]
	v_pk_mul_f32 v[148:149], v[18:19], v[18:19]
	v_mov_b32_e32 v150, v146
	v_mov_b32_e32 v151, v148
	v_mov_b32_e32 v148, v147
	v_pk_add_f32 v[146:147], v[150:151], v[148:149]
	v_lshlrev_b32_e32 v170, 7, v209
	v_add_f32_e32 v147, v152, v147
	v_add_f32_e32 v210, v146, v147
	ds_read_b128 v[146:149], v245 offset:52224
	s_nop 0
	ds_read_b128 v[150:153], v244 offset:52224
	s_nop 0
	ds_read_b128 v[154:157], v245 offset:19456
	s_nop 0
	ds_read_b128 v[158:161], v244 offset:19456
	v_pk_mul_f32 v[184:185], v[8:9], v[8:9]
	v_pk_mul_f32 v[204:205], v[6:7], v[6:7]
	v_mov_b32_e32 v206, v184
	v_mov_b32_e32 v207, v204
	v_mov_b32_e32 v204, v185
	v_pk_add_f32 v[184:185], v[206:207], v[204:205]
	v_pk_mul_f32 v[204:205], v[2:3], v[2:3]
	v_add_f32_e32 v170, v210, v185
	v_add_f32_e32 v170, v184, v170
	v_pk_mul_f32 v[184:185], v[4:5], v[4:5]
	v_mov_b32_e32 v207, v204
	v_mov_b32_e32 v206, v184
	v_mov_b32_e32 v204, v185
	v_pk_add_f32 v[184:185], v[206:207], v[204:205]
	s_nop 0
	v_add_f32_e32 v170, v185, v170
	v_add_f32_e32 v170, v184, v170
	ds_bpermute_b32 v184, v201, v170
	s_waitcnt lgkmcnt(0)
	v_add_f32_e32 v170, v170, v184
	ds_bpermute_b32 v184, v202, v170
	s_waitcnt lgkmcnt(0)
	v_add_f32_e32 v170, v170, v184
	v_fmamk_f32 v170, v170, 0x3c800000, v195
	v_mul_f32_e32 v184, 0x4f800000, v170
	v_cmp_gt_f32_e32 vcc, s70, v170
	s_nop 1
	v_cndmask_b32_e32 v170, v170, v184, vcc
	v_sqrt_f32_e32 v184, v170
	s_nop 0
	v_add_u32_e32 v185, -1, v184
	v_fma_f32 v201, -v185, v184, v170
	v_cmp_ge_f32_e64 s[4:5], 0, v201
	v_add_u32_e32 v201, 1, v184
	s_nop 0
	v_cndmask_b32_e64 v185, v184, v185, s[4:5]
	v_fma_f32 v184, -v201, v184, v170
	v_cmp_lt_f32_e64 s[4:5], 0, v184
	s_nop 1
	v_cndmask_b32_e64 v184, v185, v201, s[4:5]
	v_mul_f32_e32 v185, 0x37800000, v184
	v_cndmask_b32_e32 v184, v184, v185, vcc
	v_cmp_class_f32_e32 vcc, v170, v196
	s_nop 1
	v_cndmask_b32_e32 v170, v184, v170, vcc
	v_div_scale_f32 v184, s[4:5], v170, v170, v200
	v_rcp_f32_e32 v185, v184
	s_nop 0
	v_fma_f32 v201, -v184, v185, 1.0
	v_fmac_f32_e32 v185, v201, v185
	v_div_scale_f32 v201, vcc, v200, v170, v200
	v_mul_f32_e32 v202, v201, v185
	v_fma_f32 v204, -v184, v202, v201
	v_fmac_f32_e32 v202, v204, v185
	v_fma_f32 v184, -v184, v202, v201
	v_div_fmas_f32 v184, v184, v185, v202
	v_div_fixup_f32 v170, v184, v170, v200
	v_pk_mul_f32 v[184:185], v[24:25], v[170:171] op_sel_hi:[1,0]
	v_pk_mul_f32 v[200:201], v[22:23], v[170:171] op_sel_hi:[1,0]
	v_pk_mul_f32 v[144:145], v[144:145], v[184:185]
	v_pk_mul_f32 v[184:185], v[20:21], v[170:171] op_sel_hi:[1,0]
	v_pk_mul_f32 v[142:143], v[142:143], v[200:201]
	v_pk_mul_f32 v[140:141], v[140:141], v[184:185]
	v_pk_mul_f32 v[184:185], v[6:7], v[170:171] op_sel_hi:[1,0]
	v_pk_mul_f32 v[200:201], v[18:19], v[170:171] op_sel_hi:[1,0]
	v_pk_mul_f32 v[134:135], v[134:135], v[184:185]
	v_pk_mul_f32 v[184:185], v[2:3], v[170:171] op_sel_hi:[1,0]
	v_pk_mul_f32 v[138:139], v[138:139], v[200:201]
	v_pk_mul_f32 v[130:131], v[130:131], v[184:185]
	v_pk_mul_f32 v[200:201], v[8:9], v[170:171] op_sel_hi:[1,0]
	s_waitcnt lgkmcnt(0)
	v_pk_mul_f32 v[204:205], v[146:147], v[130:131]
	s_waitcnt lgkmcnt(0)
	v_pk_mul_f32 v[130:131], v[154:155], v[130:131]
	v_pk_mul_f32 v[136:137], v[136:137], v[200:201]
	v_pk_mul_f32 v[200:201], v[4:5], v[170:171] op_sel_hi:[1,0]
	v_pk_fma_f32 v[204:205], v[154:155], v[138:139], v[204:205] neg_lo:[0,0,1] neg_hi:[0,0,1]
	v_pk_fma_f32 v[138:139], v[146:147], v[138:139], v[130:131]
	v_lshlrev_b32_e32 v130, 6, v209
	v_lshlrev_b32_e32 v131, 3, v208
	v_pk_mul_f32 v[132:133], v[132:133], v[200:201]
	v_and_b32_e32 v130, s37, v130
	v_and_b32_e32 v131, s9, v131
	v_pk_mul_f32 v[184:185], v[150:151], v[134:135]
	v_pk_mul_f32 v[200:201], v[152:153], v[136:137]
	v_pk_mul_f32 v[206:207], v[148:149], v[132:133]
	v_or3_b32 v130, v131, v203, v130
	s_waitcnt lgkmcnt(0)
	v_pk_fma_f32 v[200:201], v[160:161], v[144:145], v[200:201] neg_lo:[0,0,1] neg_hi:[0,0,1]
	v_pk_fma_f32 v[184:185], v[158:159], v[142:143], v[184:185] neg_lo:[0,0,1] neg_hi:[0,0,1]
	v_pk_fma_f32 v[206:207], v[156:157], v[140:141], v[206:207] neg_lo:[0,0,1] neg_hi:[0,0,1]
	v_pk_mul_f32 v[134:135], v[158:159], v[134:135]
	v_pk_mul_f32 v[136:137], v[160:161], v[136:137]
	v_pk_mul_f32 v[132:133], v[156:157], v[132:133]
	v_ashrrev_i32_e32 v131, 31, v130
	v_pk_fma_f32 v[136:137], v[152:153], v[144:145], v[136:137]
	v_pk_fma_f32 v[134:135], v[150:151], v[142:143], v[134:135]
	v_pk_fma_f32 v[140:141], v[148:149], v[140:141], v[132:133]
	v_lshl_add_u64 v[142:143], v[130:131], 1, s[6:7]
	v_cvt_pk_f16_f32 v130, v184, v185
	v_cvt_pk_f16_f32 v131, v200, v201
	v_cvt_pk_f16_f32 v132, v204, v205
	v_cvt_pk_f16_f32 v133, v206, v207
	v_cvt_pk_f16_f32 v134, v134, v135
	v_cvt_pk_f16_f32 v135, v136, v137
	v_cvt_pk_f16_f32 v136, v138, v139
	v_cvt_pk_f16_f32 v137, v140, v141
	global_store_dwordx4 v[142:143], v[130:133], off sc1
	s_nop 1
	v_lshl_add_u64 v[130:131], v[142:143], 0, s[10:11]
	global_store_dwordx4 v[130:131], v[134:137], off sc1
	s_branch .LBB1_14

	.amdhsa_kernel _Z15gemm_qkv_kernelPKDF16_S0_PDF16_S1_S1_PKfS3_S3_S3_S3_S1_PKiPyPj
		.amdhsa_group_segment_fixed_size 0
		.amdhsa_private_segment_fixed_size 0
		.amdhsa_kernarg_size 112
		.amdhsa_user_sgpr_count 2
		.amdhsa_user_sgpr_dispatch_ptr 0
		.amdhsa_user_sgpr_queue_ptr 0
		.amdhsa_user_sgpr_kernarg_segment_ptr 1
		.amdhsa_user_sgpr_dispatch_id 0
		.amdhsa_user_sgpr_kernarg_preload_length 0
		.amdhsa_user_sgpr_kernarg_preload_offset 0
		.amdhsa_user_sgpr_private_segment_size 0
		.amdhsa_uses_dynamic_stack 0
		.amdhsa_enable_private_segment 0
		.amdhsa_system_sgpr_workgroup_id_x 1
		.amdhsa_system_sgpr_workgroup_id_y 0
		.amdhsa_system_sgpr_workgroup_id_z 0
		.amdhsa_system_sgpr_workgroup_info 0
		.amdhsa_system_vgpr_workitem_id 0
		.amdhsa_next_free_vgpr 248
		.amdhsa_next_free_sgpr 94
		.amdhsa_accum_offset 248
		.amdhsa_reserve_vcc 1
		.amdhsa_float_round_mode_32 0
		.amdhsa_float_round_mode_16_64 0
		.amdhsa_float_denorm_mode_32 3
		.amdhsa_float_denorm_mode_16_64 3
		.amdhsa_dx10_clamp 1
		.amdhsa_ieee_mode 1
		.amdhsa_fp16_overflow 0
		.amdhsa_tg_split 0
		.amdhsa_exception_fp_ieee_invalid_op 0
		.amdhsa_exception_fp_denorm_src 0
		.amdhsa_exception_fp_ieee_div_zero 0
		.amdhsa_exception_fp_ieee_overflow 0
		.amdhsa_exception_fp_ieee_underflow 0
		.amdhsa_exception_fp_ieee_inexact 0
		.amdhsa_exception_int_div_zero 0
	.end_amdhsa_kernel

amdhsa.kernels:
  - .agpr_count:     0
    .args:
      - .actual_access:  read_only
        .address_space:  global
        .offset:         0
        .size:           8
        .value_kind:     global_buffer
      - .actual_access:  read_only
        .address_space:  global
        .offset:         8
        .size:           8
        .value_kind:     global_buffer
      - .actual_access:  read_only
        .address_space:  global
        .offset:         16
        .size:           8
        .value_kind:     global_buffer
      - .actual_access:  write_only
        .address_space:  global
        .offset:         24
        .size:           8
        .value_kind:     global_buffer
      - .actual_access:  write_only
        .address_space:  global
        .offset:         32
        .size:           8
        .value_kind:     global_buffer
      - .actual_access:  write_only
        .address_space:  global
        .offset:         40
        .size:           8
        .value_kind:     global_buffer
      - .actual_access:  write_only
        .address_space:  global
        .offset:         48
        .size:           8
        .value_kind:     global_buffer
    .group_segment_fixed_size: 0
    .kernarg_segment_align: 8
    .kernarg_segment_size: 56
    .language:       OpenCL C
    .language_version:
      - 2
      - 0
    .max_flat_workgroup_size: 1024
    .name:           _Z11prep_kernelPKfS0_PKiPDF16_S3_PfS4_
    .private_segment_fixed_size: 0
    .sgpr_count:     24
    .sgpr_spill_count: 0
    .symbol:         _Z11prep_kernelPKfS0_PKiPDF16_S3_PfS4_.kd
    .uniform_work_group_size: 1
    .uses_dynamic_stack: false
    .vgpr_count:     40
    .vgpr_spill_count: 0
    .wavefront_size: 64
  - .agpr_count:     0
    .args:
      - .address_space:  global
        .offset:         0
        .size:           8
        .value_kind:     global_buffer
      - .address_space:  global
        .offset:         8
        .size:           8
        .value_kind:     global_buffer
      - .address_space:  global
        .offset:         16
        .size:           8
        .value_kind:     global_buffer
      - .address_space:  global
        .offset:         24
        .size:           8
        .value_kind:     global_buffer
      - .address_space:  global
        .offset:         32
        .size:           8
        .value_kind:     global_buffer
      - .address_space:  global
        .offset:         40
        .size:           8
        .value_kind:     global_buffer
      - .address_space:  global
        .offset:         48
        .size:           8
        .value_kind:     global_buffer
      - .address_space:  global
        .offset:         56
        .size:           8
        .value_kind:     global_buffer
      - .address_space:  global
        .offset:         64
        .size:           8
        .value_kind:     global_buffer
      - .address_space:  global
        .offset:         72
        .size:           8
        .value_kind:     global_buffer
      - .address_space:  global
        .offset:         80
        .size:           8
        .value_kind:     global_buffer
      - .address_space:  global
        .offset:         88
        .size:           8
        .value_kind:     global_buffer
      - .address_space:  global
        .offset:         96
        .size:           8
        .value_kind:     global_buffer
      - .address_space:  global
        .offset:         104
        .size:           8
        .value_kind:     global_buffer
    .group_segment_fixed_size: 0
    .kernarg_segment_align: 8
    .kernarg_segment_size: 112
    .language:       OpenCL C
    .language_version:
      - 2
      - 0
    .max_flat_workgroup_size: 512
    .name:           _Z15gemm_qkv_kernelPKDF16_S0_PDF16_S1_S1_PKfS3_S3_S3_S3_S1_PKiPyPj
    .private_segment_fixed_size: 0
    .sgpr_count:     100
    .sgpr_spill_count: 0
    .symbol:         _Z15gemm_qkv_kernelPKDF16_S0_PDF16_S1_S1_PKfS3_S3_S3_S3_S1_PKiPyPj.kd
    .uniform_work_group_size: 1
    .uses_dynamic_stack: false
    .vgpr_count:     248
    .vgpr_spill_count: 0
    .wavefront_size: 64
  - .agpr_count:     0
    .args:
      - .address_space:  global
        .offset:         0
        .size:           8
        .value_kind:     global_buffer
      - .address_space:  global
        .offset:         8
        .size:           8
        .value_kind:     global_buffer
      - .address_space:  global
        .offset:         16
        .size:           8
        .value_kind:     global_buffer
    .group_segment_fixed_size: 0
    .kernarg_segment_align: 8
    .kernarg_segment_size: 24
    .language:       OpenCL C
    .language_version:
      - 2
      - 0
    .max_flat_workgroup_size: 512
    .name:           _Z15gemm_out_kernelPKDF16_S0_Pf
    .private_segment_fixed_size: 0
    .sgpr_count:     26
    .sgpr_spill_count: 0
    .symbol:         _Z15gemm_out_kernelPKDF16_S0_Pf.kd
    .uniform_work_group_size: 1
    .uses_dynamic_stack: false
    .vgpr_count:     148
    .vgpr_spill_count: 0
    .wavefront_size: 64
  - .agpr_count:     0
    .args:
      - .address_space:  global
        .offset:         0
        .size:           8
        .value_kind:     global_buffer
      - .address_space:  global
        .offset:         8
        .size:           8
        .value_kind:     global_buffer
      - .address_space:  global
        .offset:         16
        .size:           8
        .value_kind:     global_buffer
      - .address_space:  global
        .offset:         24
        .size:           8
        .value_kind:     global_buffer
      - .address_space:  global
        .offset:         32
        .size:           8
        .value_kind:     global_buffer
      - .address_space:  global
        .offset:         40
        .size:           8
        .value_kind:     global_buffer
    .group_segment_fixed_size: 0
    .kernarg_segment_align: 8
    .kernarg_segment_size: 48
    .language:       OpenCL C
    .language_version:
      - 2
      - 0
    .max_flat_workgroup_size: 512
    .name:           _Z11attn_kernelPKDF16_S0_S0_PDF16_PKjS3_
    .private_segment_fixed_size: 0
    .sgpr_count:     68
    .sgpr_spill_count: 0
    .symbol:         _Z11attn_kernelPKDF16_S0_S0_PDF16_PKjS3_.kd
    .uniform_work_group_size: 1
    .uses_dynamic_stack: false
    .vgpr_count:     248
    .vgpr_spill_count: 0
    .wavefront_size: 64
